# P7 residual epilogue: x loads batched per 128-row half, stores back-to-back (on top of mLSTM S^T read hoist)
# speedup vs baseline: 1.0098x; 1.0098x over previous
; __device__ __forceinline__ unsigned pk2(float lo, float hi) { const f32x2 v = {lo, hi}; const bf16x2_t b = __builtin_convertvector(v, bf16x2_t); return __builtin_bit_cast(unsigned, b); }
;     __device__ __forceinline__ void operator()(const f32x4 (&acc)[2][2][4][2], const Unit& u, int wr, int wc, int fr, int fq) const {
;         const int row0 = u.pm * BM + wr * 64 + fr, col0 = u.pn * BM + wc * 32 + 8 * fq;
; #pragma unroll
;         for (int ai = 0; ai < 2; ++ai)
; #pragma unroll
;             for (int m = 0; m < 4; ++m) { const size_t off = (size_t)(row0 + ai * HALF + m * 16) * D + col0;
; #pragma unroll
;                 for (int bj = 0; bj < 2; ++bj) { const f32x4 v0 = *(const f32x4*)(X + off + bj * HALF) + acc[ai][bj][m][0], v1 = *(const f32x4*)(X + off + bj * HALF + 4) + acc[ai][bj][m][1];
;                     v4u w; w.x = pk2(v0[0], v0[1]); w.y = pk2(v0[2], v0[3]); w.z = pk2(v1[0], v1[1]); w.w = pk2(v1[2], v1[3]);
;                     *(v4u*)(O + off + bj * HALF) = w; } }
;     }
.LBB0_1364:
	v_lshl_add_u32 v164, s28, 8, v1
	v_lshl_or_b32 v166, s52, 8, v149
	v_ashrrev_i32_e32 v165, 31, v164
	v_readlane_b32 s52, v237, 0
	v_ashrrev_i32_e32 v167, 31, v166
	v_lshlrev_b64 v[146:147], 11, v[164:165]
	v_readlane_b32 s53, v237, 1
	v_lshl_add_u64 v[146:147], v[146:147], 0, v[166:167]
	s_mov_b64 s[36:37], s[52:53]
	v_lshl_add_u64 v[168:169], v[146:147], 2, s[36:37]
	v_lshl_add_u64 v[170:171], v[146:147], 1, s[6:7]
	s_andn2_b64 vcc, exec, s[4:5]
	s_mov_b64 s[4:5], -1
	v_readlane_b32 s54, v237, 2
	v_readlane_b32 s55, v237, 3
	v_readlane_b32 s56, v237, 4
	v_readlane_b32 s57, v237, 5
	v_readlane_b32 s58, v237, 6
	v_readlane_b32 s59, v237, 7
	v_readlane_b32 s60, v237, 8
	v_readlane_b32 s61, v237, 9
	v_readlane_b32 s62, v237, 10
	v_readlane_b32 s63, v237, 11
	v_readlane_b32 s64, v237, 12
	v_readlane_b32 s65, v237, 13
	v_readlane_b32 s66, v237, 14
	v_readlane_b32 s67, v237, 15
	s_mov_b32 s98, 0x20000
	s_mov_b32 s99, 0
	s_mov_b32 s100, 0x10000
	s_mov_b32 s101, 0
	v_mov_b64_e32 v[154:155], v[168:169]
	global_load_dwordx4 v[172:175], v[154:155], off
	global_load_dwordx4 v[176:179], v[154:155], off offset:16
	global_load_dwordx4 v[180:183], v[154:155], off offset:512
	global_load_dwordx4 v[184:187], v[154:155], off offset:528
	v_lshl_add_u64 v[154:155], v[154:155], 0, s[98:99]
	global_load_dwordx4 v[188:191], v[154:155], off
	global_load_dwordx4 v[192:195], v[154:155], off offset:16
	global_load_dwordx4 v[196:199], v[154:155], off offset:512
	global_load_dwordx4 v[200:203], v[154:155], off offset:528
	v_lshl_add_u64 v[154:155], v[154:155], 0, s[98:99]
	global_load_dwordx4 v[204:207], v[154:155], off
	global_load_dwordx4 v[208:211], v[154:155], off offset:16
	global_load_dwordx4 v[212:215], v[154:155], off offset:512
	global_load_dwordx4 v[216:219], v[154:155], off offset:528
	v_lshl_add_u64 v[154:155], v[154:155], 0, s[98:99]
	global_load_dwordx4 v[220:223], v[154:155], off
	global_load_dwordx4 v[224:227], v[154:155], off offset:16
	global_load_dwordx4 v[228:231], v[154:155], off offset:512
	global_load_dwordx4 v[232:235], v[154:155], off offset:528
	s_waitcnt vmcnt(0)
	v_mov_b64_e32 v[156:157], v[170:171]
	v_pk_add_f32 v[124:125], v[124:125], v[178:179]
	v_pk_add_f32 v[122:123], v[122:123], v[176:177]
	v_pk_add_f32 v[126:127], v[126:127], v[172:173]
	v_pk_add_f32 v[128:129], v[128:129], v[174:175]
	v_cvt_pk_bf16_f32 v125, v124, v125
	v_cvt_pk_bf16_f32 v124, v122, v123
	v_cvt_pk_bf16_f32 v122, v126, v127
	v_cvt_pk_bf16_f32 v123, v128, v129
	global_store_dwordx4 v[156:157], v[122:125], off
	v_pk_add_f32 v[116:117], v[116:117], v[186:187]
	v_pk_add_f32 v[114:115], v[114:115], v[184:185]
	v_pk_add_f32 v[118:119], v[118:119], v[180:181]
	v_pk_add_f32 v[120:121], v[120:121], v[182:183]
	v_cvt_pk_bf16_f32 v117, v116, v117
	v_cvt_pk_bf16_f32 v116, v114, v115
	v_cvt_pk_bf16_f32 v114, v118, v119
	v_cvt_pk_bf16_f32 v115, v120, v121
	global_store_dwordx4 v[156:157], v[114:117], off offset:256
	v_lshl_add_u64 v[156:157], v[156:157], 0, s[100:101]
	v_pk_add_f32 v[108:109], v[108:109], v[194:195]
	v_pk_add_f32 v[106:107], v[106:107], v[192:193]
	v_pk_add_f32 v[110:111], v[110:111], v[188:189]
	v_pk_add_f32 v[112:113], v[112:113], v[190:191]
	v_cvt_pk_bf16_f32 v109, v108, v109
	v_cvt_pk_bf16_f32 v108, v106, v107
	v_cvt_pk_bf16_f32 v106, v110, v111
	v_cvt_pk_bf16_f32 v107, v112, v113
	global_store_dwordx4 v[156:157], v[106:109], off
	v_pk_add_f32 v[100:101], v[100:101], v[202:203]
	v_pk_add_f32 v[98:99], v[98:99], v[200:201]
	v_pk_add_f32 v[102:103], v[102:103], v[196:197]
	v_pk_add_f32 v[104:105], v[104:105], v[198:199]
	v_cvt_pk_bf16_f32 v101, v100, v101
	v_cvt_pk_bf16_f32 v100, v98, v99
	v_cvt_pk_bf16_f32 v98, v102, v103
	v_cvt_pk_bf16_f32 v99, v104, v105
	global_store_dwordx4 v[156:157], v[98:101], off offset:256
	v_lshl_add_u64 v[156:157], v[156:157], 0, s[100:101]
	v_pk_add_f32 v[92:93], v[92:93], v[210:211]
	v_pk_add_f32 v[90:91], v[90:91], v[208:209]
	v_pk_add_f32 v[94:95], v[94:95], v[204:205]
	v_pk_add_f32 v[96:97], v[96:97], v[206:207]
	v_cvt_pk_bf16_f32 v93, v92, v93
	v_cvt_pk_bf16_f32 v92, v90, v91
	v_cvt_pk_bf16_f32 v90, v94, v95
	v_cvt_pk_bf16_f32 v91, v96, v97
	global_store_dwordx4 v[156:157], v[90:93], off
	v_pk_add_f32 v[84:85], v[84:85], v[218:219]
	v_pk_add_f32 v[82:83], v[82:83], v[216:217]
	v_pk_add_f32 v[86:87], v[86:87], v[212:213]
	v_pk_add_f32 v[88:89], v[88:89], v[214:215]
	v_cvt_pk_bf16_f32 v85, v84, v85
	v_cvt_pk_bf16_f32 v84, v82, v83
	v_cvt_pk_bf16_f32 v82, v86, v87
	v_cvt_pk_bf16_f32 v83, v88, v89
	global_store_dwordx4 v[156:157], v[82:85], off offset:256
	v_lshl_add_u64 v[156:157], v[156:157], 0, s[100:101]
	v_pk_add_f32 v[76:77], v[76:77], v[226:227]
	v_pk_add_f32 v[74:75], v[74:75], v[224:225]
	v_pk_add_f32 v[78:79], v[78:79], v[220:221]
	v_pk_add_f32 v[80:81], v[80:81], v[222:223]
	v_cvt_pk_bf16_f32 v77, v76, v77
	v_cvt_pk_bf16_f32 v76, v74, v75
	v_cvt_pk_bf16_f32 v74, v78, v79
	v_cvt_pk_bf16_f32 v75, v80, v81
	global_store_dwordx4 v[156:157], v[74:77], off
	v_pk_add_f32 v[68:69], v[68:69], v[234:235]
	v_pk_add_f32 v[66:67], v[66:67], v[232:233]
	v_pk_add_f32 v[70:71], v[70:71], v[228:229]
	v_pk_add_f32 v[72:73], v[72:73], v[230:231]
	v_cvt_pk_bf16_f32 v69, v68, v69
	v_cvt_pk_bf16_f32 v68, v66, v67
	v_cvt_pk_bf16_f32 v66, v70, v71
	v_cvt_pk_bf16_f32 v67, v72, v73
	global_store_dwordx4 v[156:157], v[66:69], off offset:256
	v_lshl_add_u64 v[154:155], s[98:99], 3, v[168:169]
	global_load_dwordx4 v[126:129], v[154:155], off
	global_load_dwordx4 v[122:125], v[154:155], off offset:16
	global_load_dwordx4 v[118:121], v[154:155], off offset:512
	global_load_dwordx4 v[114:117], v[154:155], off offset:528
	v_lshl_add_u64 v[154:155], v[154:155], 0, s[98:99]
	global_load_dwordx4 v[110:113], v[154:155], off
	global_load_dwordx4 v[106:109], v[154:155], off offset:16
	global_load_dwordx4 v[102:105], v[154:155], off offset:512
	global_load_dwordx4 v[98:101], v[154:155], off offset:528
	v_lshl_add_u64 v[154:155], v[154:155], 0, s[98:99]
	global_load_dwordx4 v[94:97], v[154:155], off
	global_load_dwordx4 v[90:93], v[154:155], off offset:16
	global_load_dwordx4 v[86:89], v[154:155], off offset:512
	global_load_dwordx4 v[82:85], v[154:155], off offset:528
	v_lshl_add_u64 v[154:155], v[154:155], 0, s[98:99]
	global_load_dwordx4 v[78:81], v[154:155], off
	global_load_dwordx4 v[74:77], v[154:155], off offset:16
	global_load_dwordx4 v[70:73], v[154:155], off offset:512
	global_load_dwordx4 v[66:69], v[154:155], off offset:528
	s_waitcnt vmcnt(0)
; __device__ __forceinline__ unsigned pk2(float lo, float hi) { const f32x2 v = {lo, hi}; const bf16x2_t b = __builtin_convertvector(v, bf16x2_t); return __builtin_bit_cast(unsigned, b); }
;     __device__ __forceinline__ void operator()(const f32x4 (&acc)[2][2][4][2], const Unit& u, int wr, int wc, int fr, int fq) const {
;         const int row0 = u.pm * BM + wr * 64 + fr, col0 = u.pn * BM + wc * 32 + 8 * fq;
; #pragma unroll
;         for (int ai = 0; ai < 2; ++ai)
; #pragma unroll
;             for (int m = 0; m < 4; ++m) { const size_t off = (size_t)(row0 + ai * HALF + m * 16) * D + col0;
; #pragma unroll
;                 for (int bj = 0; bj < 2; ++bj) { const f32x4 v0 = *(const f32x4*)(X + off + bj * HALF) + acc[ai][bj][m][0], v1 = *(const f32x4*)(X + off + bj * HALF + 4) + acc[ai][bj][m][1];
;                     v4u w; w.x = pk2(v0[0], v0[1]); w.y = pk2(v0[2], v0[3]); w.z = pk2(v1[0], v1[1]); w.w = pk2(v1[2], v1[3]);
;                     *(v4u*)(O + off + bj * HALF) = w; } }
;     }
	v_lshl_add_u64 v[156:157], s[100:101], 3, v[170:171]
	v_pk_add_f32 v[60:61], v[60:61], v[124:125]
	v_pk_add_f32 v[58:59], v[58:59], v[122:123]
	v_pk_add_f32 v[62:63], v[62:63], v[126:127]
	v_pk_add_f32 v[64:65], v[64:65], v[128:129]
	v_cvt_pk_bf16_f32 v61, v60, v61
	v_cvt_pk_bf16_f32 v60, v58, v59
	v_cvt_pk_bf16_f32 v58, v62, v63
	v_cvt_pk_bf16_f32 v59, v64, v65
	global_store_dwordx4 v[156:157], v[58:61], off
	v_pk_add_f32 v[52:53], v[52:53], v[116:117]
	v_pk_add_f32 v[50:51], v[50:51], v[114:115]
	v_pk_add_f32 v[54:55], v[54:55], v[118:119]
	v_pk_add_f32 v[56:57], v[56:57], v[120:121]
	v_cvt_pk_bf16_f32 v53, v52, v53
	v_cvt_pk_bf16_f32 v52, v50, v51
	v_cvt_pk_bf16_f32 v50, v54, v55
	v_cvt_pk_bf16_f32 v51, v56, v57
	global_store_dwordx4 v[156:157], v[50:53], off offset:256
	v_lshl_add_u64 v[156:157], v[156:157], 0, s[100:101]
	v_pk_add_f32 v[44:45], v[44:45], v[108:109]
	v_pk_add_f32 v[42:43], v[42:43], v[106:107]
	v_pk_add_f32 v[46:47], v[46:47], v[110:111]
	v_pk_add_f32 v[48:49], v[48:49], v[112:113]
	v_cvt_pk_bf16_f32 v45, v44, v45
	v_cvt_pk_bf16_f32 v44, v42, v43
	v_cvt_pk_bf16_f32 v42, v46, v47
	v_cvt_pk_bf16_f32 v43, v48, v49
	global_store_dwordx4 v[156:157], v[42:45], off
	v_pk_add_f32 v[36:37], v[36:37], v[100:101]
	v_pk_add_f32 v[34:35], v[34:35], v[98:99]
	v_pk_add_f32 v[38:39], v[38:39], v[102:103]
	v_pk_add_f32 v[40:41], v[40:41], v[104:105]
	v_cvt_pk_bf16_f32 v37, v36, v37
	v_cvt_pk_bf16_f32 v36, v34, v35
	v_cvt_pk_bf16_f32 v34, v38, v39
	v_cvt_pk_bf16_f32 v35, v40, v41
	global_store_dwordx4 v[156:157], v[34:37], off offset:256
	v_lshl_add_u64 v[156:157], v[156:157], 0, s[100:101]
	v_pk_add_f32 v[28:29], v[28:29], v[92:93]
	v_pk_add_f32 v[26:27], v[26:27], v[90:91]
	v_pk_add_f32 v[30:31], v[30:31], v[94:95]
	v_pk_add_f32 v[32:33], v[32:33], v[96:97]
	v_cvt_pk_bf16_f32 v29, v28, v29
	v_cvt_pk_bf16_f32 v28, v26, v27
	v_cvt_pk_bf16_f32 v26, v30, v31
	v_cvt_pk_bf16_f32 v27, v32, v33
	global_store_dwordx4 v[156:157], v[26:29], off
	v_pk_add_f32 v[20:21], v[20:21], v[84:85]
	v_pk_add_f32 v[18:19], v[18:19], v[82:83]
	v_pk_add_f32 v[22:23], v[22:23], v[86:87]
	v_pk_add_f32 v[24:25], v[24:25], v[88:89]
	v_cvt_pk_bf16_f32 v21, v20, v21
	v_cvt_pk_bf16_f32 v20, v18, v19
	v_cvt_pk_bf16_f32 v18, v22, v23
	v_cvt_pk_bf16_f32 v19, v24, v25
	global_store_dwordx4 v[156:157], v[18:21], off offset:256
	v_lshl_add_u64 v[156:157], v[156:157], 0, s[100:101]
	v_pk_add_f32 v[12:13], v[12:13], v[76:77]
	v_pk_add_f32 v[10:11], v[10:11], v[74:75]
	v_pk_add_f32 v[14:15], v[14:15], v[78:79]
	v_pk_add_f32 v[16:17], v[16:17], v[80:81]
	v_cvt_pk_bf16_f32 v13, v12, v13
	v_cvt_pk_bf16_f32 v12, v10, v11
	v_cvt_pk_bf16_f32 v10, v14, v15
	v_cvt_pk_bf16_f32 v11, v16, v17
	global_store_dwordx4 v[156:157], v[10:13], off
	v_pk_add_f32 v[4:5], v[4:5], v[68:69]
	v_pk_add_f32 v[2:3], v[2:3], v[66:67]
	v_pk_add_f32 v[6:7], v[6:7], v[70:71]
	v_pk_add_f32 v[8:9], v[8:9], v[72:73]
	v_cvt_pk_bf16_f32 v5, v4, v5
	v_cvt_pk_bf16_f32 v4, v2, v3
	v_cvt_pk_bf16_f32 v2, v6, v7
	v_cvt_pk_bf16_f32 v3, v8, v9
	global_store_dwordx4 v[156:157], v[2:5], off offset:256
	s_cbranch_vccnz .LBB0_1353
	s_andn2_b64 vcc, exec, s[2:3]
	s_cbranch_vccnz .LBB0_1352
	s_barrier
	s_branch .LBB0_1352

; __global__ void __launch_bounds__(NTHR, 2) mk_fwd(Args args) {
	.amdhsa_kernel _Z6mk_fwd4Args
		.amdhsa_group_segment_fixed_size 0
		.amdhsa_private_segment_fixed_size 0
		.amdhsa_kernarg_size 520
		.amdhsa_user_sgpr_count 2
		.amdhsa_user_sgpr_dispatch_ptr 0
		.amdhsa_user_sgpr_queue_ptr 0
		.amdhsa_user_sgpr_kernarg_segment_ptr 1
		.amdhsa_user_sgpr_dispatch_id 0
		.amdhsa_user_sgpr_kernarg_preload_length 0
		.amdhsa_user_sgpr_kernarg_preload_offset 0
		.amdhsa_user_sgpr_private_segment_size 0
		.amdhsa_uses_dynamic_stack 0
		.amdhsa_enable_private_segment 0
		.amdhsa_system_sgpr_workgroup_id_x 1
		.amdhsa_system_sgpr_workgroup_id_y 0
		.amdhsa_system_sgpr_workgroup_id_z 0
		.amdhsa_system_sgpr_workgroup_info 0
		.amdhsa_system_vgpr_workitem_id 0
		.amdhsa_next_free_vgpr 248
		.amdhsa_next_free_sgpr 102
		.amdhsa_accum_offset 248
		.amdhsa_reserve_vcc 1
		.amdhsa_float_round_mode_32 0
		.amdhsa_float_round_mode_16_64 0
		.amdhsa_float_denorm_mode_32 3
		.amdhsa_float_denorm_mode_16_64 3
		.amdhsa_dx10_clamp 1
		.amdhsa_ieee_mode 1
		.amdhsa_fp16_overflow 0
		.amdhsa_tg_split 0
		.amdhsa_exception_fp_ieee_invalid_op 0
		.amdhsa_exception_fp_denorm_src 0
		.amdhsa_exception_fp_ieee_div_zero 0
		.amdhsa_exception_fp_ieee_overflow 0
		.amdhsa_exception_fp_ieee_underflow 0
		.amdhsa_exception_fp_ieee_inexact 0
		.amdhsa_exception_int_div_zero 0
	.end_amdhsa_kernel

; __global__ void __launch_bounds__(NTHR, 2) mk_fwd(Args args) {
amdhsa.kernels:
  - .agpr_count:     0
    .args:
      - .offset:         0
        .size:           264
        .value_kind:     by_value
      - .offset:         264
        .size:           4
        .value_kind:     hidden_block_count_x
      - .offset:         268
        .size:           4
        .value_kind:     hidden_block_count_y
      - .offset:         272
        .size:           4
        .value_kind:     hidden_block_count_z
      - .offset:         276
        .size:           2
        .value_kind:     hidden_group_size_x
      - .offset:         278
        .size:           2
        .value_kind:     hidden_group_size_y
      - .offset:         280
        .size:           2
        .value_kind:     hidden_group_size_z
      - .offset:         282
        .size:           2
        .value_kind:     hidden_remainder_x
      - .offset:         284
        .size:           2
        .value_kind:     hidden_remainder_y
      - .offset:         286
        .size:           2
        .value_kind:     hidden_remainder_z
      - .offset:         304
        .size:           8
        .value_kind:     hidden_global_offset_x
      - .offset:         312
        .size:           8
        .value_kind:     hidden_global_offset_y
      - .offset:         320
        .size:           8
        .value_kind:     hidden_global_offset_z
      - .offset:         328
        .size:           2
        .value_kind:     hidden_grid_dims
      - .offset:         384
        .size:           4
        .value_kind:     hidden_dynamic_lds_size
    .group_segment_fixed_size: 0
    .kernarg_segment_align: 8
    .kernarg_segment_size: 520
    .language:       OpenCL C
    .language_version:
      - 2
      - 0
    .max_flat_workgroup_size: 512
    .name:           _Z6mk_fwd4Args
    .private_segment_fixed_size: 0
    .sgpr_count:     108
    .sgpr_spill_count: 126
    .symbol:         _Z6mk_fwd4Args.kd
    .uniform_work_group_size: 1
    .uses_dynamic_stack: false
    .vgpr_count:     248
    .vgpr_spill_count: 0
    .wavefront_size: 64
